# copy routine (nt) + trimmed mixer-phase copy shares moved to idle workgroups of the layer-0 P5/P9 tails + padding-row MFMA skip
# speedup vs baseline: 1.0098x; 1.0044x over previous
.LBB0_1363:
.LBB0_1365:
.LBB0_1366:
.LBB0_1368:
.LBB0_1370:
.LBB0_1372:
.LBB0_1374:
.LBB0_1378:
.LBB0_1380:
.LBB0_1381:
.LBB0_1383:
.LBB0_1385:
.LBB0_1387:
.LBB0_1388:
.LBB0_1390:
.LBB0_1392:
.LBB0_1393:
.LBB0_1394:
.LBB0_1395:
.LBB0_1397:
.LBB0_1401:
.LBB0_1403:
.LBB0_1404:
.LBB0_1406:
.LBB0_1408:
.LBB0_1410:
.LBB0_1411:
.LBB0_1414:
.LBB0_1418:
.LBB0_1420:
.LBB0_1421:
.LBB0_1423:
.LBB0_1425:
.Lmoe_site_A:
	s_nop 1
	v_writelane_b32 v255, s0, 0
	v_writelane_b32 v255, s1, 1
	v_writelane_b32 v255, s2, 2
	v_writelane_b32 v255, s3, 3
	v_writelane_b32 v255, s4, 4
	v_writelane_b32 v255, s5, 5
	v_writelane_b32 v255, s6, 6
	v_writelane_b32 v255, s7, 7
	v_writelane_b32 v255, s8, 8
	v_writelane_b32 v255, s9, 9
	v_writelane_b32 v255, s10, 10
	v_writelane_b32 v255, s11, 11
	v_writelane_b32 v255, s12, 12
	v_writelane_b32 v255, s13, 13
	v_writelane_b32 v255, s14, 14
	v_writelane_b32 v255, s15, 15
	v_writelane_b32 v255, s16, 16
	v_writelane_b32 v255, s17, 17
	v_writelane_b32 v255, s18, 18
	v_writelane_b32 v255, s19, 19
	v_writelane_b32 v255, s20, 20
	v_writelane_b32 v255, s21, 21
	v_writelane_b32 v255, s22, 22
	v_writelane_b32 v255, s23, 23
	v_writelane_b32 v255, s24, 24
	v_writelane_b32 v255, s25, 25
	v_writelane_b32 v255, s26, 26
	v_writelane_b32 v255, s27, 27
	v_writelane_b32 v255, s28, 28
	v_writelane_b32 v255, s29, 29
	v_writelane_b32 v255, s30, 30
	v_writelane_b32 v255, s31, 31
	v_writelane_b32 v255, s32, 32
	v_writelane_b32 v255, s33, 33
	v_writelane_b32 v255, s34, 34
	v_writelane_b32 v255, s35, 35
	s_movk_i32 s0, 0
	s_movk_i32 s2, 16
	s_mov_b32 s4, 0x7800
	s_mov_b32 s5, 0xe200
	s_mov_b32 s34, 0xe400
	s_branch .Lmoe_p4
.Lmoe_site_B:
	s_nop 1
	v_writelane_b32 v255, s0, 0
	v_writelane_b32 v255, s1, 1
	v_writelane_b32 v255, s2, 2
	v_writelane_b32 v255, s3, 3
	v_writelane_b32 v255, s4, 4
	v_writelane_b32 v255, s5, 5
	v_writelane_b32 v255, s6, 6
	v_writelane_b32 v255, s7, 7
	v_writelane_b32 v255, s8, 8
	v_writelane_b32 v255, s9, 9
	v_writelane_b32 v255, s10, 10
	v_writelane_b32 v255, s11, 11
	v_writelane_b32 v255, s12, 12
	v_writelane_b32 v255, s13, 13
	v_writelane_b32 v255, s14, 14
	v_writelane_b32 v255, s15, 15
	v_writelane_b32 v255, s16, 16
	v_writelane_b32 v255, s17, 17
	v_writelane_b32 v255, s18, 18
	v_writelane_b32 v255, s19, 19
	v_writelane_b32 v255, s20, 20
	v_writelane_b32 v255, s21, 21
	v_writelane_b32 v255, s22, 22
	v_writelane_b32 v255, s23, 23
	v_writelane_b32 v255, s24, 24
	v_writelane_b32 v255, s25, 25
	v_writelane_b32 v255, s26, 26
	v_writelane_b32 v255, s27, 27
	v_writelane_b32 v255, s28, 28
	v_writelane_b32 v255, s29, 29
	v_writelane_b32 v255, s30, 30
	v_writelane_b32 v255, s31, 31
	v_writelane_b32 v255, s32, 32
	v_writelane_b32 v255, s33, 33
	v_writelane_b32 v255, s34, 34
	v_writelane_b32 v255, s35, 35
	s_movk_i32 s0, 1
	s_movk_i32 s2, 8
	s_mov_b32 s4, 0x800
	s_mov_b32 s5, 0x6600
	s_mov_b32 s34, 0x6800
	s_branch .Lmoe_p4
.Lmoe_site_D:
	s_nop 1
	v_writelane_b32 v255, s0, 0
	v_writelane_b32 v255, s1, 1
	v_writelane_b32 v255, s2, 2
	v_writelane_b32 v255, s3, 3
	v_writelane_b32 v255, s4, 4
	v_writelane_b32 v255, s5, 5
	v_writelane_b32 v255, s6, 6
	v_writelane_b32 v255, s7, 7
	v_writelane_b32 v255, s8, 8
	v_writelane_b32 v255, s9, 9
	v_writelane_b32 v255, s10, 10
	v_writelane_b32 v255, s11, 11
	v_writelane_b32 v255, s12, 12
	v_writelane_b32 v255, s13, 13
	v_writelane_b32 v255, s14, 14
	v_writelane_b32 v255, s15, 15
	v_writelane_b32 v255, s16, 16
	v_writelane_b32 v255, s17, 17
	v_writelane_b32 v255, s18, 18
	v_writelane_b32 v255, s19, 19
	v_writelane_b32 v255, s20, 20
	v_writelane_b32 v255, s21, 21
	v_writelane_b32 v255, s22, 22
	v_writelane_b32 v255, s23, 23
	v_writelane_b32 v255, s24, 24
	v_writelane_b32 v255, s25, 25
	v_writelane_b32 v255, s26, 26
	v_writelane_b32 v255, s27, 27
	v_writelane_b32 v255, s28, 28
	v_writelane_b32 v255, s29, 29
	v_writelane_b32 v255, s30, 30
	v_writelane_b32 v255, s31, 31
	v_writelane_b32 v255, s32, 32
	v_writelane_b32 v255, s33, 33
	v_writelane_b32 v255, s34, 34
	v_writelane_b32 v255, s35, 35
	s_movk_i32 s0, 2
	s_movk_i32 s2, 0
	s_mov_b32 s4, 0x0
	s_mov_b32 s5, 0x800
	s_mov_b32 s34, 0x800
	s_branch .Lmoe_p4
.Lmoe_site_E:
	s_nop 1
	v_writelane_b32 v255, s0, 0
	v_writelane_b32 v255, s1, 1
	v_writelane_b32 v255, s2, 2
	v_writelane_b32 v255, s3, 3
	v_writelane_b32 v255, s4, 4
	v_writelane_b32 v255, s5, 5
	v_writelane_b32 v255, s6, 6
	v_writelane_b32 v255, s7, 7
	v_writelane_b32 v255, s8, 8
	v_writelane_b32 v255, s9, 9
	v_writelane_b32 v255, s10, 10
	v_writelane_b32 v255, s11, 11
	v_writelane_b32 v255, s12, 12
	v_writelane_b32 v255, s13, 13
	v_writelane_b32 v255, s14, 14
	v_writelane_b32 v255, s15, 15
	v_writelane_b32 v255, s16, 16
	v_writelane_b32 v255, s17, 17
	v_writelane_b32 v255, s18, 18
	v_writelane_b32 v255, s19, 19
	v_writelane_b32 v255, s20, 20
	v_writelane_b32 v255, s21, 21
	v_writelane_b32 v255, s22, 22
	v_writelane_b32 v255, s23, 23
	v_writelane_b32 v255, s24, 24
	v_writelane_b32 v255, s25, 25
	v_writelane_b32 v255, s26, 26
	v_writelane_b32 v255, s27, 27
	v_writelane_b32 v255, s28, 28
	v_writelane_b32 v255, s29, 29
	v_writelane_b32 v255, s30, 30
	v_writelane_b32 v255, s31, 31
	v_writelane_b32 v255, s32, 32
	v_writelane_b32 v255, s33, 33
	v_writelane_b32 v255, s34, 34
	v_writelane_b32 v255, s35, 35
	s_movk_i32 s0, 3
	s_movk_i32 s2, 24
	s_mov_b32 s4, 0xfc00
	s_mov_b32 s5, 0x16600
	s_mov_b32 s34, 0x16800
	s_branch .Lmoe_p4
.Lmoe_site_T1:
	s_nop 1
	v_writelane_b32 v255, s0, 0
	v_writelane_b32 v255, s1, 1
	v_writelane_b32 v255, s2, 2
	v_writelane_b32 v255, s3, 3
	v_writelane_b32 v255, s4, 4
	v_writelane_b32 v255, s5, 5
	v_writelane_b32 v255, s6, 6
	v_writelane_b32 v255, s7, 7
	v_writelane_b32 v255, s8, 8
	v_writelane_b32 v255, s9, 9
	v_writelane_b32 v255, s10, 10
	v_writelane_b32 v255, s11, 11
	v_writelane_b32 v255, s12, 12
	v_writelane_b32 v255, s13, 13
	v_writelane_b32 v255, s14, 14
	v_writelane_b32 v255, s15, 15
	v_writelane_b32 v255, s16, 16
	v_writelane_b32 v255, s17, 17
	v_writelane_b32 v255, s18, 18
	v_writelane_b32 v255, s19, 19
	v_writelane_b32 v255, s20, 20
	v_writelane_b32 v255, s21, 21
	v_writelane_b32 v255, s22, 22
	v_writelane_b32 v255, s23, 23
	v_writelane_b32 v255, s24, 24
	v_writelane_b32 v255, s25, 25
	v_writelane_b32 v255, s26, 26
	v_writelane_b32 v255, s27, 27
	v_writelane_b32 v255, s28, 28
	v_writelane_b32 v255, s29, 29
	v_writelane_b32 v255, s30, 30
	v_writelane_b32 v255, s31, 31
	v_writelane_b32 v255, s32, 32
	v_writelane_b32 v255, s33, 33
	v_writelane_b32 v255, s34, 34
	v_writelane_b32 v255, s35, 35
	s_movk_i32 s0, 4
	v_readlane_b32 s20, v252, 32
	s_nop 3
	s_cmp_eq_u32 s20, 0
	s_cbranch_scc1 .Lmoe_T1_l1
	s_movk_i32 s2, 32
	s_movk_i32 s26, 1792
	s_mov_b32 s27, 0x1200
	s_mov_b32 s28, 0x2c00
	s_mov_b32 s29, 0x6600
	s_mov_b32 s32, 0xd000
	s_mov_b32 s33, 0x13a00
	s_mov_b32 s5, 0x4600
	s_branch .Lmoe_tail
.Lmoe_T1_l1:
	s_mov_b64 s[30:31], exec
	s_branch .Lmoe_exit
.Lmoe_site_T2:
	s_nop 1
	v_writelane_b32 v255, s0, 0
	v_writelane_b32 v255, s1, 1
	v_writelane_b32 v255, s2, 2
	v_writelane_b32 v255, s3, 3
	v_writelane_b32 v255, s4, 4
	v_writelane_b32 v255, s5, 5
	v_writelane_b32 v255, s6, 6
	v_writelane_b32 v255, s7, 7
	v_writelane_b32 v255, s8, 8
	v_writelane_b32 v255, s9, 9
	v_writelane_b32 v255, s10, 10
	v_writelane_b32 v255, s11, 11
	v_writelane_b32 v255, s12, 12
	v_writelane_b32 v255, s13, 13
	v_writelane_b32 v255, s14, 14
	v_writelane_b32 v255, s15, 15
	v_writelane_b32 v255, s16, 16
	v_writelane_b32 v255, s17, 17
	v_writelane_b32 v255, s18, 18
	v_writelane_b32 v255, s19, 19
	v_writelane_b32 v255, s20, 20
	v_writelane_b32 v255, s21, 21
	v_writelane_b32 v255, s22, 22
	v_writelane_b32 v255, s23, 23
	v_writelane_b32 v255, s24, 24
	v_writelane_b32 v255, s25, 25
	v_writelane_b32 v255, s26, 26
	v_writelane_b32 v255, s27, 27
	v_writelane_b32 v255, s28, 28
	v_writelane_b32 v255, s29, 29
	v_writelane_b32 v255, s30, 30
	v_writelane_b32 v255, s31, 31
	v_writelane_b32 v255, s32, 32
	v_writelane_b32 v255, s33, 33
	v_writelane_b32 v255, s34, 34
	v_writelane_b32 v255, s35, 35
	s_movk_i32 s0, 5
	v_readlane_b32 s20, v252, 32
	s_nop 3
	s_cmp_eq_u32 s20, 0
	s_cbranch_scc1 .Lmoe_T2_l1
	s_movk_i32 s2, 128
	s_movk_i32 s26, 1024
	s_mov_b32 s27, 0x1000
	s_mov_b32 s28, 0x2800
	s_mov_b32 s29, 0x1e800
	s_mov_b32 s32, 0x25400
	s_mov_b32 s33, 0x2c000
	s_mov_b32 s5, 0x4000
	s_branch .Lmoe_tail

.Lmoe_site_T3:
.Lmoe_T3_l1:
.Lmoe_tail:
	s_mov_b64 s[30:31], exec
	s_mov_b64 exec, -1
	v_lshrrev_b32_e32 v16, 6, v0
	v_and_b32_e32 v17, 63, v0
	v_readlane_b32 s20, v252, 32
	v_readfirstlane_b32 s1, v16
	v_readlane_b32 s6, v253, 14
	v_readlane_b32 s7, v253, 15
	s_nop 3
	s_cmp_lt_u32 s90, s2
	s_cbranch_scc1 .Lmoe_exit
	s_sub_u32 s21, s90, s2
	s_lshl_b32 s21, s21, 3
	s_add_u32 s4, s21, s1
	s_branch .Lmoe_common
.Lmoe_p4:
	s_mov_b64 s[30:31], exec
	s_mov_b64 exec, -1
	v_lshrrev_b32_e32 v16, 6, v0
	v_and_b32_e32 v17, 63, v0
	v_readlane_b32 s20, v252, 32
	v_readfirstlane_b32 s1, v16
	v_readlane_b32 s6, v253, 14
	v_readlane_b32 s7, v253, 15
	s_nop 3
	s_cmp_eq_u32 s20, 0
	s_cselect_b32 s20, 0x18000, 0
	s_cselect_b32 s5, s34, s5
	s_add_u32 s4, s4, s20
	s_add_u32 s5, s5, s20
	s_and_b32 s21, s90, 7
	s_lshr_b32 s22, s90, 3
	s_lshl_b32 s21, s21, 3
	s_add_u32 s21, s21, s22
	s_sub_u32 s21, s21, s2
	s_lshl_b32 s21, s21, 3
	s_add_u32 s21, s21, s1
	s_add_u32 s4, s4, s21
	s_movk_i32 s26, 0x200
	s_mov_b32 s27, -1
	s_mov_b32 s28, -1
	s_mov_b32 s29, 0
	s_mov_b32 s32, 0
	s_mov_b32 s33, 0
.Lmoe_common:
	s_mov_b32 s14, s4
	v_mov_b32_e32 v18, 0x24190
	ds_read_b64 v[20:21], v18
	ds_read_b64 v[22:23], v18 offset:8
	ds_read_b64 v[24:25], v18 offset:16
	v_lshrrev_b32_e32 v19, 3, v17
	v_and_b32_e32 v26, 7, v17
	v_lshlrev_b32_e32 v27, 13, v19
	v_lshl_add_u32 v27, v26, 4, v27
	v_mov_b32_e32 v160, v27
	v_add_u32_e32 v161, 0x10000, v27
	v_add_u32_e32 v162, 0x20000, v27
	v_add_u32_e32 v163, 0x30000, v27
	v_add_u32_e32 v164, 0x40000, v27
	v_add_u32_e32 v165, 0x50000, v27
	v_add_u32_e32 v166, 0x60000, v27
	v_add_u32_e32 v167, 0x70000, v27
	v_lshlrev_b32_e32 v28, 12, v19
	v_lshl_add_u32 v28, v26, 4, v28
	v_mov_b32_e32 v168, v28
	v_add_u32_e32 v169, 0x8000, v28
	v_add_u32_e32 v170, 0x10000, v28
	v_add_u32_e32 v171, 0x18000, v28
	s_mul_i32 s21, s1, 0x4100
	v_lshlrev_b32_e32 v172, 4, v17
	v_add_u32_e32 v172, s21, v172
	v_mul_u32_u24_e32 v173, 0x410, v26
	v_lshl_add_u32 v173, v19, 2, v173
	v_add_u32_e32 v173, s21, v173
	s_waitcnt lgkmcnt(0)
	v_readfirstlane_b32 s8, v20
	v_readfirstlane_b32 s9, v21
	v_readfirstlane_b32 s10, v22
	v_readfirstlane_b32 s11, v23
	v_readfirstlane_b32 s12, v24
	v_readfirstlane_b32 s13, v25
	s_mov_b32 s15, 0
	s_mov_b32 s3, 0
	s_nop 3
	s_cmp_ge_u32 s4, s5
	s_cbranch_scc1 .Lmoe_drain_entry
	s_cmp_lt_u32 s4, s27
	s_cselect_b32 s21, s29, s32
	s_cmp_lt_u32 s4, s28
	s_cselect_b32 s21, s21, s33
	s_add_u32 s22, s4, s21
	s_cmp_ge_u32 s22, 0x18000
	s_cselect_b32 s20, 1, 0
	s_mul_i32 s21, s20, 0x18000
	s_sub_u32 s21, s22, s21
	s_lshr_b32 s22, s21, 15
	s_bfe_u32 s23, s21, 0x4000b
	s_lshl_b32 s20, s20, 4
	s_add_u32 s23, s23, s20
	s_lshl_b32 s23, s23, 24
	s_bfe_u32 s20, s21, 0x50006
	s_lshl_b32 s20, s20, 19
	s_add_u32 s23, s23, s20
	s_and_b32 s20, s21, 63
	s_lshl_b32 s20, s20, 7
	s_add_u32 s23, s23, s20
	s_cmp_eq_u32 s22, 0
	s_cselect_b32 s16, s8, s10
	s_cselect_b32 s17, s9, s11
	s_cmp_eq_u32 s22, 2
	s_cselect_b32 s16, s12, s16
	s_cselect_b32 s17, s13, s17
	s_add_u32 s16, s16, s23
	s_addc_u32 s17, s17, 0
	global_load_dwordx4 v[44:47], v160, s[16:17] nt
	global_load_dwordx4 v[48:51], v161, s[16:17] nt
	global_load_dwordx4 v[52:55], v162, s[16:17] nt
	global_load_dwordx4 v[56:59], v163, s[16:17] nt
	global_load_dwordx4 v[60:63], v164, s[16:17] nt
	global_load_dwordx4 v[64:67], v165, s[16:17] nt
	global_load_dwordx4 v[68:71], v166, s[16:17] nt
	global_load_dwordx4 v[72:75], v167, s[16:17] nt
	s_add_u32 s4, s4, s26
	s_add_u32 s3, s3, 1
	s_cmp_ge_u32 s4, s5
	s_cbranch_scc1 .Lmoe_drain_entry
	s_cmp_lt_u32 s4, s27
	s_cselect_b32 s21, s29, s32
	s_cmp_lt_u32 s4, s28
	s_cselect_b32 s21, s21, s33
	s_add_u32 s22, s4, s21
	s_cmp_ge_u32 s22, 0x18000
	s_cselect_b32 s20, 1, 0
	s_mul_i32 s21, s20, 0x18000
	s_sub_u32 s21, s22, s21
	s_lshr_b32 s22, s21, 15
	s_bfe_u32 s23, s21, 0x4000b
	s_lshl_b32 s20, s20, 4
	s_add_u32 s23, s23, s20
	s_lshl_b32 s23, s23, 24
	s_bfe_u32 s20, s21, 0x50006
	s_lshl_b32 s20, s20, 19
	s_add_u32 s23, s23, s20
	s_and_b32 s20, s21, 63
	s_lshl_b32 s20, s20, 7
	s_add_u32 s23, s23, s20
	s_cmp_eq_u32 s22, 0
	s_cselect_b32 s16, s8, s10
	s_cselect_b32 s17, s9, s11
	s_cmp_eq_u32 s22, 2
	s_cselect_b32 s16, s12, s16
	s_cselect_b32 s17, s13, s17
	s_add_u32 s16, s16, s23
	s_addc_u32 s17, s17, 0
	global_load_dwordx4 v[76:79], v160, s[16:17] nt
	global_load_dwordx4 v[80:83], v161, s[16:17] nt
	global_load_dwordx4 v[84:87], v162, s[16:17] nt
	global_load_dwordx4 v[88:91], v163, s[16:17] nt
	global_load_dwordx4 v[92:95], v164, s[16:17] nt
	global_load_dwordx4 v[96:99], v165, s[16:17] nt
	global_load_dwordx4 v[100:103], v166, s[16:17] nt
	global_load_dwordx4 v[104:107], v167, s[16:17] nt
	s_add_u32 s4, s4, s26
	s_add_u32 s3, s3, 1
	s_cmp_ge_u32 s4, s5
	s_cbranch_scc1 .Lmoe_drain_entry
	s_cmp_lt_u32 s4, s27
	s_cselect_b32 s21, s29, s32
	s_cmp_lt_u32 s4, s28
	s_cselect_b32 s21, s21, s33
	s_add_u32 s22, s4, s21
	s_cmp_ge_u32 s22, 0x18000
	s_cselect_b32 s20, 1, 0
	s_mul_i32 s21, s20, 0x18000
	s_sub_u32 s21, s22, s21
	s_lshr_b32 s22, s21, 15
	s_bfe_u32 s23, s21, 0x4000b
	s_lshl_b32 s20, s20, 4
	s_add_u32 s23, s23, s20
	s_lshl_b32 s23, s23, 24
	s_bfe_u32 s20, s21, 0x50006
	s_lshl_b32 s20, s20, 19
	s_add_u32 s23, s23, s20
	s_and_b32 s20, s21, 63
	s_lshl_b32 s20, s20, 7
	s_add_u32 s23, s23, s20
	s_cmp_eq_u32 s22, 0
	s_cselect_b32 s16, s8, s10
	s_cselect_b32 s17, s9, s11
	s_cmp_eq_u32 s22, 2
	s_cselect_b32 s16, s12, s16
	s_cselect_b32 s17, s13, s17
	s_add_u32 s16, s16, s23
	s_addc_u32 s17, s17, 0
	global_load_dwordx4 v[108:111], v160, s[16:17] nt
	global_load_dwordx4 v[112:115], v161, s[16:17] nt
	global_load_dwordx4 v[116:119], v162, s[16:17] nt
	global_load_dwordx4 v[120:123], v163, s[16:17] nt
	global_load_dwordx4 v[124:127], v164, s[16:17] nt
	global_load_dwordx4 v[128:131], v165, s[16:17] nt
	global_load_dwordx4 v[132:135], v166, s[16:17] nt
	global_load_dwordx4 v[136:139], v167, s[16:17] nt
	s_add_u32 s4, s4, s26
	s_add_u32 s3, s3, 1
	s_cmp_ge_u32 s4, s5
	s_cbranch_scc1 .Lmoe_drain_entry
	s_cmp_lt_u32 s4, s27
	s_cselect_b32 s21, s29, s32
	s_cmp_lt_u32 s4, s28
	s_cselect_b32 s21, s21, s33
	s_add_u32 s22, s4, s21
	s_cmp_ge_u32 s22, 0x18000
	s_cselect_b32 s20, 1, 0
	s_mul_i32 s21, s20, 0x18000
	s_sub_u32 s21, s22, s21
	s_lshr_b32 s22, s21, 15
	s_bfe_u32 s23, s21, 0x4000b
	s_lshl_b32 s20, s20, 4
	s_add_u32 s23, s23, s20
	s_lshl_b32 s23, s23, 24
	s_bfe_u32 s20, s21, 0x50006
	s_lshl_b32 s20, s20, 19
	s_add_u32 s23, s23, s20
	s_and_b32 s20, s21, 63
	s_lshl_b32 s20, s20, 7
	s_add_u32 s23, s23, s20
	s_cmp_eq_u32 s22, 0
	s_cselect_b32 s16, s8, s10
	s_cselect_b32 s17, s9, s11
	s_cmp_eq_u32 s22, 2
	s_cselect_b32 s16, s12, s16
	s_cselect_b32 s17, s13, s17
	s_add_u32 s16, s16, s23
	s_addc_u32 s17, s17, 0
	global_load_dwordx4 v[224:227], v160, s[16:17] nt
	global_load_dwordx4 v[228:231], v161, s[16:17] nt
	global_load_dwordx4 v[232:235], v162, s[16:17] nt
	global_load_dwordx4 v[236:239], v163, s[16:17] nt
	global_load_dwordx4 v[240:243], v164, s[16:17] nt
	global_load_dwordx4 v[244:247], v165, s[16:17] nt
	global_load_dwordx4 v[248:251], v166, s[16:17] nt
	global_load_dwordx4 v[216:219], v167, s[16:17] nt
	s_add_u32 s4, s4, s26
	s_add_u32 s3, s3, 1

.Lmoe_go_0:
	s_cmp_lt_u32 s14, s27
	s_cselect_b32 s21, s29, s32
	s_cmp_lt_u32 s14, s28
	s_cselect_b32 s21, s21, s33
	s_add_u32 s22, s14, s21
	s_cmp_ge_u32 s22, 0x18000
	s_cselect_b32 s20, 1, 0
	s_mul_i32 s21, s20, 0x18000
	s_sub_u32 s21, s22, s21
	s_lshr_b32 s22, s21, 15
	s_bfe_u32 s23, s21, 0x4000b
	s_lshl_b32 s20, s20, 4
	s_add_u32 s23, s23, s20
	s_bfe_u32 s24, s21, 0x50006
	s_lshl_b32 s24, s24, 7
	s_and_b32 s25, s21, 63
	s_cmp_eq_u32 s22, 2
	s_cbranch_scc1 .Lmoe_dstd_0
	s_lshl_b32 s23, s23, 24
	s_lshl_b32 s22, s22, 19
	s_add_u32 s23, s23, s22
	s_lshr_b32 s22, s25, 2
	s_lshl_b32 s22, s22, 20
	s_add_u32 s23, s23, s22
	s_and_b32 s22, s25, 3
	s_lshl_b32 s22, s22, 17
	s_add_u32 s23, s23, s22
	s_add_u32 s23, s23, s24
	s_add_u32 s23, s23, 0x3840000
	s_branch .Lmoe_dste_0

.Lmoe_dste_0:
	s_add_u32 s18, s6, s23
	s_addc_u32 s19, s7, 0
	ds_write_b128 v172, v[44:47] offset:0
	ds_write_b128 v172, v[48:51] offset:1040
	ds_write_b128 v172, v[52:55] offset:2080
	ds_write_b128 v172, v[56:59] offset:3120
	ds_write_b128 v172, v[60:63] offset:4160
	ds_write_b128 v172, v[64:67] offset:5200
	ds_write_b128 v172, v[68:71] offset:6240
	ds_write_b128 v172, v[72:75] offset:7280
	s_waitcnt lgkmcnt(0)
	ds_read2_b32 v[44:45], v173 offset0:0 offset1:32
	ds_read2_b32 v[46:47], v173 offset0:64 offset1:96
	ds_read2_b32 v[48:49], v173 offset0:128 offset1:160
	ds_read2_b32 v[50:51], v173 offset0:192 offset1:224
	ds_read2_b32 v[52:53], v173 offset0:8 offset1:40
	ds_read2_b32 v[54:55], v173 offset0:72 offset1:104
	ds_read2_b32 v[56:57], v173 offset0:136 offset1:168
	ds_read2_b32 v[58:59], v173 offset0:200 offset1:232
	ds_read2_b32 v[60:61], v173 offset0:16 offset1:48
	ds_read2_b32 v[62:63], v173 offset0:80 offset1:112
	ds_read2_b32 v[64:65], v173 offset0:144 offset1:176
	ds_read2_b32 v[66:67], v173 offset0:208 offset1:240
	s_waitcnt lgkmcnt(8)
	v_cvt_pk_bf16_f32 v44, v44, v45
	v_cvt_pk_bf16_f32 v45, v46, v47
	v_cvt_pk_bf16_f32 v46, v48, v49
	v_cvt_pk_bf16_f32 v47, v50, v51
	global_store_dwordx4 v168, v[44:47], s[18:19] nt
	ds_read2_b32 v[68:69], v173 offset0:24 offset1:56
	ds_read2_b32 v[70:71], v173 offset0:88 offset1:120
	ds_read2_b32 v[72:73], v173 offset0:152 offset1:184
	ds_read2_b32 v[74:75], v173 offset0:216 offset1:248
	s_waitcnt lgkmcnt(8)
	v_cvt_pk_bf16_f32 v52, v52, v53
	v_cvt_pk_bf16_f32 v53, v54, v55
	v_cvt_pk_bf16_f32 v54, v56, v57
	v_cvt_pk_bf16_f32 v55, v58, v59
	global_store_dwordx4 v169, v[52:55], s[18:19] nt
	s_waitcnt lgkmcnt(4)
	v_cvt_pk_bf16_f32 v60, v60, v61
	v_cvt_pk_bf16_f32 v61, v62, v63
	v_cvt_pk_bf16_f32 v62, v64, v65
	v_cvt_pk_bf16_f32 v63, v66, v67
	global_store_dwordx4 v170, v[60:63], s[18:19] nt
	s_waitcnt lgkmcnt(0)
	v_cvt_pk_bf16_f32 v68, v68, v69
	v_cvt_pk_bf16_f32 v69, v70, v71
	v_cvt_pk_bf16_f32 v70, v72, v73
	v_cvt_pk_bf16_f32 v71, v74, v75
	global_store_dwordx4 v171, v[68:71], s[18:19] nt
	s_add_u32 s14, s14, s26
	s_add_u32 s15, s15, 1
	s_cmp_ge_u32 s4, s5
	s_cbranch_scc1 .Lmoe_drain3_1
	s_cmp_lt_u32 s4, s27
	s_cselect_b32 s21, s29, s32
	s_cmp_lt_u32 s4, s28
	s_cselect_b32 s21, s21, s33
	s_add_u32 s22, s4, s21
	s_cmp_ge_u32 s22, 0x18000
	s_cselect_b32 s20, 1, 0
	s_mul_i32 s21, s20, 0x18000
	s_sub_u32 s21, s22, s21
	s_lshr_b32 s22, s21, 15
	s_bfe_u32 s23, s21, 0x4000b
	s_lshl_b32 s20, s20, 4
	s_add_u32 s23, s23, s20
	s_lshl_b32 s23, s23, 24
	s_bfe_u32 s20, s21, 0x50006
	s_lshl_b32 s20, s20, 19
	s_add_u32 s23, s23, s20
	s_and_b32 s20, s21, 63
	s_lshl_b32 s20, s20, 7
	s_add_u32 s23, s23, s20
	s_cmp_eq_u32 s22, 0
	s_cselect_b32 s16, s8, s10
	s_cselect_b32 s17, s9, s11
	s_cmp_eq_u32 s22, 2
	s_cselect_b32 s16, s12, s16
	s_cselect_b32 s17, s13, s17
	s_add_u32 s16, s16, s23
	s_addc_u32 s17, s17, 0
	global_load_dwordx4 v[44:47], v160, s[16:17] nt
	global_load_dwordx4 v[48:51], v161, s[16:17] nt
	global_load_dwordx4 v[52:55], v162, s[16:17] nt
	global_load_dwordx4 v[56:59], v163, s[16:17] nt
	global_load_dwordx4 v[60:63], v164, s[16:17] nt
	global_load_dwordx4 v[64:67], v165, s[16:17] nt
	global_load_dwordx4 v[68:71], v166, s[16:17] nt
	global_load_dwordx4 v[72:75], v167, s[16:17] nt
	s_add_u32 s4, s4, s26
	s_cmp_lt_u32 s15, 3
	s_cbranch_scc1 .Lmoe_w24_1
	s_waitcnt vmcnt(36)
	s_branch .Lmoe_go_1

.Lmoe_dste_1:
	s_add_u32 s18, s6, s23
	s_addc_u32 s19, s7, 0
	ds_write_b128 v172, v[76:79] offset:0
	ds_write_b128 v172, v[80:83] offset:1040
	ds_write_b128 v172, v[84:87] offset:2080
	ds_write_b128 v172, v[88:91] offset:3120
	ds_write_b128 v172, v[92:95] offset:4160
	ds_write_b128 v172, v[96:99] offset:5200
	ds_write_b128 v172, v[100:103] offset:6240
	ds_write_b128 v172, v[104:107] offset:7280
	s_waitcnt lgkmcnt(0)
	ds_read2_b32 v[76:77], v173 offset0:0 offset1:32
	ds_read2_b32 v[78:79], v173 offset0:64 offset1:96
	ds_read2_b32 v[80:81], v173 offset0:128 offset1:160
	ds_read2_b32 v[82:83], v173 offset0:192 offset1:224
	ds_read2_b32 v[84:85], v173 offset0:8 offset1:40
	ds_read2_b32 v[86:87], v173 offset0:72 offset1:104
	ds_read2_b32 v[88:89], v173 offset0:136 offset1:168
	ds_read2_b32 v[90:91], v173 offset0:200 offset1:232
	ds_read2_b32 v[92:93], v173 offset0:16 offset1:48
	ds_read2_b32 v[94:95], v173 offset0:80 offset1:112
	ds_read2_b32 v[96:97], v173 offset0:144 offset1:176
	ds_read2_b32 v[98:99], v173 offset0:208 offset1:240
	s_waitcnt lgkmcnt(8)
	v_cvt_pk_bf16_f32 v76, v76, v77
	v_cvt_pk_bf16_f32 v77, v78, v79
	v_cvt_pk_bf16_f32 v78, v80, v81
	v_cvt_pk_bf16_f32 v79, v82, v83
	global_store_dwordx4 v168, v[76:79], s[18:19] nt
	ds_read2_b32 v[100:101], v173 offset0:24 offset1:56
	ds_read2_b32 v[102:103], v173 offset0:88 offset1:120
	ds_read2_b32 v[104:105], v173 offset0:152 offset1:184
	ds_read2_b32 v[106:107], v173 offset0:216 offset1:248
	s_waitcnt lgkmcnt(8)
	v_cvt_pk_bf16_f32 v84, v84, v85
	v_cvt_pk_bf16_f32 v85, v86, v87
	v_cvt_pk_bf16_f32 v86, v88, v89
	v_cvt_pk_bf16_f32 v87, v90, v91
	global_store_dwordx4 v169, v[84:87], s[18:19] nt
	s_waitcnt lgkmcnt(4)
	v_cvt_pk_bf16_f32 v92, v92, v93
	v_cvt_pk_bf16_f32 v93, v94, v95
	v_cvt_pk_bf16_f32 v94, v96, v97
	v_cvt_pk_bf16_f32 v95, v98, v99
	global_store_dwordx4 v170, v[92:95], s[18:19] nt
	s_waitcnt lgkmcnt(0)
	v_cvt_pk_bf16_f32 v100, v100, v101
	v_cvt_pk_bf16_f32 v101, v102, v103
	v_cvt_pk_bf16_f32 v102, v104, v105
	v_cvt_pk_bf16_f32 v103, v106, v107
	global_store_dwordx4 v171, v[100:103], s[18:19] nt
	s_add_u32 s14, s14, s26
	s_add_u32 s15, s15, 1
	s_cmp_ge_u32 s4, s5
	s_cbranch_scc1 .Lmoe_drain3_2
	s_cmp_lt_u32 s4, s27
	s_cselect_b32 s21, s29, s32
	s_cmp_lt_u32 s4, s28
	s_cselect_b32 s21, s21, s33
	s_add_u32 s22, s4, s21
	s_cmp_ge_u32 s22, 0x18000
	s_cselect_b32 s20, 1, 0
	s_mul_i32 s21, s20, 0x18000
	s_sub_u32 s21, s22, s21
	s_lshr_b32 s22, s21, 15
	s_bfe_u32 s23, s21, 0x4000b
	s_lshl_b32 s20, s20, 4
	s_add_u32 s23, s23, s20
	s_lshl_b32 s23, s23, 24
	s_bfe_u32 s20, s21, 0x50006
	s_lshl_b32 s20, s20, 19
	s_add_u32 s23, s23, s20
	s_and_b32 s20, s21, 63
	s_lshl_b32 s20, s20, 7
	s_add_u32 s23, s23, s20
	s_cmp_eq_u32 s22, 0
	s_cselect_b32 s16, s8, s10
	s_cselect_b32 s17, s9, s11
	s_cmp_eq_u32 s22, 2
	s_cselect_b32 s16, s12, s16
	s_cselect_b32 s17, s13, s17
	s_add_u32 s16, s16, s23
	s_addc_u32 s17, s17, 0
	global_load_dwordx4 v[76:79], v160, s[16:17] nt
	global_load_dwordx4 v[80:83], v161, s[16:17] nt
	global_load_dwordx4 v[84:87], v162, s[16:17] nt
	global_load_dwordx4 v[88:91], v163, s[16:17] nt
	global_load_dwordx4 v[92:95], v164, s[16:17] nt
	global_load_dwordx4 v[96:99], v165, s[16:17] nt
	global_load_dwordx4 v[100:103], v166, s[16:17] nt
	global_load_dwordx4 v[104:107], v167, s[16:17] nt
	s_add_u32 s4, s4, s26
	s_cmp_lt_u32 s15, 3
	s_cbranch_scc1 .Lmoe_w24_2
	s_waitcnt vmcnt(36)
	s_branch .Lmoe_go_2

.Lmoe_dste_2:
	s_add_u32 s18, s6, s23
	s_addc_u32 s19, s7, 0
	ds_write_b128 v172, v[108:111] offset:0
	ds_write_b128 v172, v[112:115] offset:1040
	ds_write_b128 v172, v[116:119] offset:2080
	ds_write_b128 v172, v[120:123] offset:3120
	ds_write_b128 v172, v[124:127] offset:4160
	ds_write_b128 v172, v[128:131] offset:5200
	ds_write_b128 v172, v[132:135] offset:6240
	ds_write_b128 v172, v[136:139] offset:7280
	s_waitcnt lgkmcnt(0)
	ds_read2_b32 v[108:109], v173 offset0:0 offset1:32
	ds_read2_b32 v[110:111], v173 offset0:64 offset1:96
	ds_read2_b32 v[112:113], v173 offset0:128 offset1:160
	ds_read2_b32 v[114:115], v173 offset0:192 offset1:224
	ds_read2_b32 v[116:117], v173 offset0:8 offset1:40
	ds_read2_b32 v[118:119], v173 offset0:72 offset1:104
	ds_read2_b32 v[120:121], v173 offset0:136 offset1:168
	ds_read2_b32 v[122:123], v173 offset0:200 offset1:232
	ds_read2_b32 v[124:125], v173 offset0:16 offset1:48
	ds_read2_b32 v[126:127], v173 offset0:80 offset1:112
	ds_read2_b32 v[128:129], v173 offset0:144 offset1:176
	ds_read2_b32 v[130:131], v173 offset0:208 offset1:240
	s_waitcnt lgkmcnt(8)
	v_cvt_pk_bf16_f32 v108, v108, v109
	v_cvt_pk_bf16_f32 v109, v110, v111
	v_cvt_pk_bf16_f32 v110, v112, v113
	v_cvt_pk_bf16_f32 v111, v114, v115
	global_store_dwordx4 v168, v[108:111], s[18:19] nt
	ds_read2_b32 v[132:133], v173 offset0:24 offset1:56
	ds_read2_b32 v[134:135], v173 offset0:88 offset1:120
	ds_read2_b32 v[136:137], v173 offset0:152 offset1:184
	ds_read2_b32 v[138:139], v173 offset0:216 offset1:248
	s_waitcnt lgkmcnt(8)
	v_cvt_pk_bf16_f32 v116, v116, v117
	v_cvt_pk_bf16_f32 v117, v118, v119
	v_cvt_pk_bf16_f32 v118, v120, v121
	v_cvt_pk_bf16_f32 v119, v122, v123
	global_store_dwordx4 v169, v[116:119], s[18:19] nt
	s_waitcnt lgkmcnt(4)
	v_cvt_pk_bf16_f32 v124, v124, v125
	v_cvt_pk_bf16_f32 v125, v126, v127
	v_cvt_pk_bf16_f32 v126, v128, v129
	v_cvt_pk_bf16_f32 v127, v130, v131
	global_store_dwordx4 v170, v[124:127], s[18:19] nt
	s_waitcnt lgkmcnt(0)
	v_cvt_pk_bf16_f32 v132, v132, v133
	v_cvt_pk_bf16_f32 v133, v134, v135
	v_cvt_pk_bf16_f32 v134, v136, v137
	v_cvt_pk_bf16_f32 v135, v138, v139
	global_store_dwordx4 v171, v[132:135], s[18:19] nt
	s_add_u32 s14, s14, s26
	s_add_u32 s15, s15, 1
	s_cmp_ge_u32 s4, s5
	s_cbranch_scc1 .Lmoe_drain3_3
	s_cmp_lt_u32 s4, s27
	s_cselect_b32 s21, s29, s32
	s_cmp_lt_u32 s4, s28
	s_cselect_b32 s21, s21, s33
	s_add_u32 s22, s4, s21
	s_cmp_ge_u32 s22, 0x18000
	s_cselect_b32 s20, 1, 0
	s_mul_i32 s21, s20, 0x18000
	s_sub_u32 s21, s22, s21
	s_lshr_b32 s22, s21, 15
	s_bfe_u32 s23, s21, 0x4000b
	s_lshl_b32 s20, s20, 4
	s_add_u32 s23, s23, s20
	s_lshl_b32 s23, s23, 24
	s_bfe_u32 s20, s21, 0x50006
	s_lshl_b32 s20, s20, 19
	s_add_u32 s23, s23, s20
	s_and_b32 s20, s21, 63
	s_lshl_b32 s20, s20, 7
	s_add_u32 s23, s23, s20
	s_cmp_eq_u32 s22, 0
	s_cselect_b32 s16, s8, s10
	s_cselect_b32 s17, s9, s11
	s_cmp_eq_u32 s22, 2
	s_cselect_b32 s16, s12, s16
	s_cselect_b32 s17, s13, s17
	s_add_u32 s16, s16, s23
	s_addc_u32 s17, s17, 0
	global_load_dwordx4 v[108:111], v160, s[16:17] nt
	global_load_dwordx4 v[112:115], v161, s[16:17] nt
	global_load_dwordx4 v[116:119], v162, s[16:17] nt
	global_load_dwordx4 v[120:123], v163, s[16:17] nt
	global_load_dwordx4 v[124:127], v164, s[16:17] nt
	global_load_dwordx4 v[128:131], v165, s[16:17] nt
	global_load_dwordx4 v[132:135], v166, s[16:17] nt
	global_load_dwordx4 v[136:139], v167, s[16:17] nt
	s_add_u32 s4, s4, s26
	s_cmp_lt_u32 s15, 3
	s_cbranch_scc1 .Lmoe_w24_3
	s_waitcnt vmcnt(36)
	s_branch .Lmoe_go_3

.Lmoe_dste_3:
	s_add_u32 s18, s6, s23
	s_addc_u32 s19, s7, 0
	ds_write_b128 v172, v[224:227] offset:0
	ds_write_b128 v172, v[228:231] offset:1040
	ds_write_b128 v172, v[232:235] offset:2080
	ds_write_b128 v172, v[236:239] offset:3120
	ds_write_b128 v172, v[240:243] offset:4160
	ds_write_b128 v172, v[244:247] offset:5200
	ds_write_b128 v172, v[248:251] offset:6240
	ds_write_b128 v172, v[216:219] offset:7280
	s_waitcnt lgkmcnt(0)
	ds_read2_b32 v[224:225], v173 offset0:0 offset1:32
	ds_read2_b32 v[226:227], v173 offset0:64 offset1:96
	ds_read2_b32 v[228:229], v173 offset0:128 offset1:160
	ds_read2_b32 v[230:231], v173 offset0:192 offset1:224
	ds_read2_b32 v[232:233], v173 offset0:8 offset1:40
	ds_read2_b32 v[234:235], v173 offset0:72 offset1:104
	ds_read2_b32 v[236:237], v173 offset0:136 offset1:168
	ds_read2_b32 v[238:239], v173 offset0:200 offset1:232
	ds_read2_b32 v[240:241], v173 offset0:16 offset1:48
	ds_read2_b32 v[242:243], v173 offset0:80 offset1:112
	ds_read2_b32 v[244:245], v173 offset0:144 offset1:176
	ds_read2_b32 v[246:247], v173 offset0:208 offset1:240
	s_waitcnt lgkmcnt(8)
	v_cvt_pk_bf16_f32 v224, v224, v225
	v_cvt_pk_bf16_f32 v225, v226, v227
	v_cvt_pk_bf16_f32 v226, v228, v229
	v_cvt_pk_bf16_f32 v227, v230, v231
	global_store_dwordx4 v168, v[224:227], s[18:19] nt
	ds_read2_b32 v[248:249], v173 offset0:24 offset1:56
	ds_read2_b32 v[250:251], v173 offset0:88 offset1:120
	ds_read2_b32 v[216:217], v173 offset0:152 offset1:184
	ds_read2_b32 v[218:219], v173 offset0:216 offset1:248
	s_waitcnt lgkmcnt(8)
	v_cvt_pk_bf16_f32 v232, v232, v233
	v_cvt_pk_bf16_f32 v233, v234, v235
	v_cvt_pk_bf16_f32 v234, v236, v237
	v_cvt_pk_bf16_f32 v235, v238, v239
	global_store_dwordx4 v169, v[232:235], s[18:19] nt
	s_waitcnt lgkmcnt(4)
	v_cvt_pk_bf16_f32 v240, v240, v241
	v_cvt_pk_bf16_f32 v241, v242, v243
	v_cvt_pk_bf16_f32 v242, v244, v245
	v_cvt_pk_bf16_f32 v243, v246, v247
	global_store_dwordx4 v170, v[240:243], s[18:19] nt
	s_waitcnt lgkmcnt(0)
	v_cvt_pk_bf16_f32 v248, v248, v249
	v_cvt_pk_bf16_f32 v249, v250, v251
	v_cvt_pk_bf16_f32 v250, v216, v217
	v_cvt_pk_bf16_f32 v251, v218, v219
	global_store_dwordx4 v171, v[248:251], s[18:19] nt
	s_add_u32 s14, s14, s26
	s_add_u32 s15, s15, 1
	s_cmp_ge_u32 s4, s5
	s_cbranch_scc1 .Lmoe_drain3_0
	s_cmp_lt_u32 s4, s27
	s_cselect_b32 s21, s29, s32
	s_cmp_lt_u32 s4, s28
	s_cselect_b32 s21, s21, s33
	s_add_u32 s22, s4, s21
	s_cmp_ge_u32 s22, 0x18000
	s_cselect_b32 s20, 1, 0
	s_mul_i32 s21, s20, 0x18000
	s_sub_u32 s21, s22, s21
	s_lshr_b32 s22, s21, 15
	s_bfe_u32 s23, s21, 0x4000b
	s_lshl_b32 s20, s20, 4
	s_add_u32 s23, s23, s20
	s_lshl_b32 s23, s23, 24
	s_bfe_u32 s20, s21, 0x50006
	s_lshl_b32 s20, s20, 19
	s_add_u32 s23, s23, s20
	s_and_b32 s20, s21, 63
	s_lshl_b32 s20, s20, 7
	s_add_u32 s23, s23, s20
	s_cmp_eq_u32 s22, 0
	s_cselect_b32 s16, s8, s10
	s_cselect_b32 s17, s9, s11
	s_cmp_eq_u32 s22, 2
	s_cselect_b32 s16, s12, s16
	s_cselect_b32 s17, s13, s17
	s_add_u32 s16, s16, s23
	s_addc_u32 s17, s17, 0
	global_load_dwordx4 v[224:227], v160, s[16:17] nt
	global_load_dwordx4 v[228:231], v161, s[16:17] nt
	global_load_dwordx4 v[232:235], v162, s[16:17] nt
	global_load_dwordx4 v[236:239], v163, s[16:17] nt
	global_load_dwordx4 v[240:243], v164, s[16:17] nt
	global_load_dwordx4 v[244:247], v165, s[16:17] nt
	global_load_dwordx4 v[248:251], v166, s[16:17] nt
	global_load_dwordx4 v[216:219], v167, s[16:17] nt
	s_add_u32 s4, s4, s26
	s_branch .Lmoe_loop

.Lmoe_drain_loop:
.Lmoe_drain_0:
	s_cmp_eq_u32 s3, 0
	s_cbranch_scc1 .Lmoe_exit
	s_cmp_lt_u32 s14, s27
	s_cselect_b32 s21, s29, s32
	s_cmp_lt_u32 s14, s28
	s_cselect_b32 s21, s21, s33
	s_add_u32 s22, s14, s21
	s_cmp_ge_u32 s22, 0x18000
	s_cselect_b32 s20, 1, 0
	s_mul_i32 s21, s20, 0x18000
	s_sub_u32 s21, s22, s21
	s_lshr_b32 s22, s21, 15
	s_bfe_u32 s23, s21, 0x4000b
	s_lshl_b32 s20, s20, 4
	s_add_u32 s23, s23, s20
	s_bfe_u32 s24, s21, 0x50006
	s_lshl_b32 s24, s24, 7
	s_and_b32 s25, s21, 63
	s_cmp_eq_u32 s22, 2
	s_cbranch_scc1 .Lmoe_dstd_4
	s_lshl_b32 s23, s23, 24
	s_lshl_b32 s22, s22, 19
	s_add_u32 s23, s23, s22
	s_lshr_b32 s22, s25, 2
	s_lshl_b32 s22, s22, 20
	s_add_u32 s23, s23, s22
	s_and_b32 s22, s25, 3
	s_lshl_b32 s22, s22, 17
	s_add_u32 s23, s23, s22
	s_add_u32 s23, s23, s24
	s_add_u32 s23, s23, 0x3840000
	s_branch .Lmoe_dste_4

.Lmoe_dste_4:
	s_add_u32 s18, s6, s23
	s_addc_u32 s19, s7, 0
	ds_write_b128 v172, v[44:47] offset:0
	ds_write_b128 v172, v[48:51] offset:1040
	ds_write_b128 v172, v[52:55] offset:2080
	ds_write_b128 v172, v[56:59] offset:3120
	ds_write_b128 v172, v[60:63] offset:4160
	ds_write_b128 v172, v[64:67] offset:5200
	ds_write_b128 v172, v[68:71] offset:6240
	ds_write_b128 v172, v[72:75] offset:7280
	s_waitcnt lgkmcnt(0)
	ds_read2_b32 v[44:45], v173 offset0:0 offset1:32
	ds_read2_b32 v[46:47], v173 offset0:64 offset1:96
	ds_read2_b32 v[48:49], v173 offset0:128 offset1:160
	ds_read2_b32 v[50:51], v173 offset0:192 offset1:224
	ds_read2_b32 v[52:53], v173 offset0:8 offset1:40
	ds_read2_b32 v[54:55], v173 offset0:72 offset1:104
	ds_read2_b32 v[56:57], v173 offset0:136 offset1:168
	ds_read2_b32 v[58:59], v173 offset0:200 offset1:232
	ds_read2_b32 v[60:61], v173 offset0:16 offset1:48
	ds_read2_b32 v[62:63], v173 offset0:80 offset1:112
	ds_read2_b32 v[64:65], v173 offset0:144 offset1:176
	ds_read2_b32 v[66:67], v173 offset0:208 offset1:240
	s_waitcnt lgkmcnt(8)
	v_cvt_pk_bf16_f32 v44, v44, v45
	v_cvt_pk_bf16_f32 v45, v46, v47
	v_cvt_pk_bf16_f32 v46, v48, v49
	v_cvt_pk_bf16_f32 v47, v50, v51
	global_store_dwordx4 v168, v[44:47], s[18:19] nt
	ds_read2_b32 v[68:69], v173 offset0:24 offset1:56
	ds_read2_b32 v[70:71], v173 offset0:88 offset1:120
	ds_read2_b32 v[72:73], v173 offset0:152 offset1:184
	ds_read2_b32 v[74:75], v173 offset0:216 offset1:248
	s_waitcnt lgkmcnt(8)
	v_cvt_pk_bf16_f32 v52, v52, v53
	v_cvt_pk_bf16_f32 v53, v54, v55
	v_cvt_pk_bf16_f32 v54, v56, v57
	v_cvt_pk_bf16_f32 v55, v58, v59
	global_store_dwordx4 v169, v[52:55], s[18:19] nt
	s_waitcnt lgkmcnt(4)
	v_cvt_pk_bf16_f32 v60, v60, v61
	v_cvt_pk_bf16_f32 v61, v62, v63
	v_cvt_pk_bf16_f32 v62, v64, v65
	v_cvt_pk_bf16_f32 v63, v66, v67
	global_store_dwordx4 v170, v[60:63], s[18:19] nt
	s_waitcnt lgkmcnt(0)
	v_cvt_pk_bf16_f32 v68, v68, v69
	v_cvt_pk_bf16_f32 v69, v70, v71
	v_cvt_pk_bf16_f32 v70, v72, v73
	v_cvt_pk_bf16_f32 v71, v74, v75
	global_store_dwordx4 v171, v[68:71], s[18:19] nt
	s_add_u32 s14, s14, s26
	s_sub_u32 s3, s3, 1
.Lmoe_drain_1:
	s_cmp_eq_u32 s3, 0
	s_cbranch_scc1 .Lmoe_exit
	s_cmp_lt_u32 s14, s27
	s_cselect_b32 s21, s29, s32
	s_cmp_lt_u32 s14, s28
	s_cselect_b32 s21, s21, s33
	s_add_u32 s22, s14, s21
	s_cmp_ge_u32 s22, 0x18000
	s_cselect_b32 s20, 1, 0
	s_mul_i32 s21, s20, 0x18000
	s_sub_u32 s21, s22, s21
	s_lshr_b32 s22, s21, 15
	s_bfe_u32 s23, s21, 0x4000b
	s_lshl_b32 s20, s20, 4
	s_add_u32 s23, s23, s20
	s_bfe_u32 s24, s21, 0x50006
	s_lshl_b32 s24, s24, 7
	s_and_b32 s25, s21, 63
	s_cmp_eq_u32 s22, 2
	s_cbranch_scc1 .Lmoe_dstd_5
	s_lshl_b32 s23, s23, 24
	s_lshl_b32 s22, s22, 19
	s_add_u32 s23, s23, s22
	s_lshr_b32 s22, s25, 2
	s_lshl_b32 s22, s22, 20
	s_add_u32 s23, s23, s22
	s_and_b32 s22, s25, 3
	s_lshl_b32 s22, s22, 17
	s_add_u32 s23, s23, s22
	s_add_u32 s23, s23, s24
	s_add_u32 s23, s23, 0x3840000
	s_branch .Lmoe_dste_5

.Lmoe_dste_5:
	s_add_u32 s18, s6, s23
	s_addc_u32 s19, s7, 0
	ds_write_b128 v172, v[76:79] offset:0
	ds_write_b128 v172, v[80:83] offset:1040
	ds_write_b128 v172, v[84:87] offset:2080
	ds_write_b128 v172, v[88:91] offset:3120
	ds_write_b128 v172, v[92:95] offset:4160
	ds_write_b128 v172, v[96:99] offset:5200
	ds_write_b128 v172, v[100:103] offset:6240
	ds_write_b128 v172, v[104:107] offset:7280
	s_waitcnt lgkmcnt(0)
	ds_read2_b32 v[76:77], v173 offset0:0 offset1:32
	ds_read2_b32 v[78:79], v173 offset0:64 offset1:96
	ds_read2_b32 v[80:81], v173 offset0:128 offset1:160
	ds_read2_b32 v[82:83], v173 offset0:192 offset1:224
	ds_read2_b32 v[84:85], v173 offset0:8 offset1:40
	ds_read2_b32 v[86:87], v173 offset0:72 offset1:104
	ds_read2_b32 v[88:89], v173 offset0:136 offset1:168
	ds_read2_b32 v[90:91], v173 offset0:200 offset1:232
	ds_read2_b32 v[92:93], v173 offset0:16 offset1:48
	ds_read2_b32 v[94:95], v173 offset0:80 offset1:112
	ds_read2_b32 v[96:97], v173 offset0:144 offset1:176
	ds_read2_b32 v[98:99], v173 offset0:208 offset1:240
	s_waitcnt lgkmcnt(8)
	v_cvt_pk_bf16_f32 v76, v76, v77
	v_cvt_pk_bf16_f32 v77, v78, v79
	v_cvt_pk_bf16_f32 v78, v80, v81
	v_cvt_pk_bf16_f32 v79, v82, v83
	global_store_dwordx4 v168, v[76:79], s[18:19] nt
	ds_read2_b32 v[100:101], v173 offset0:24 offset1:56
	ds_read2_b32 v[102:103], v173 offset0:88 offset1:120
	ds_read2_b32 v[104:105], v173 offset0:152 offset1:184
	ds_read2_b32 v[106:107], v173 offset0:216 offset1:248
	s_waitcnt lgkmcnt(8)
	v_cvt_pk_bf16_f32 v84, v84, v85
	v_cvt_pk_bf16_f32 v85, v86, v87
	v_cvt_pk_bf16_f32 v86, v88, v89
	v_cvt_pk_bf16_f32 v87, v90, v91
	global_store_dwordx4 v169, v[84:87], s[18:19] nt
	s_waitcnt lgkmcnt(4)
	v_cvt_pk_bf16_f32 v92, v92, v93
	v_cvt_pk_bf16_f32 v93, v94, v95
	v_cvt_pk_bf16_f32 v94, v96, v97
	v_cvt_pk_bf16_f32 v95, v98, v99
	global_store_dwordx4 v170, v[92:95], s[18:19] nt
	s_waitcnt lgkmcnt(0)
	v_cvt_pk_bf16_f32 v100, v100, v101
	v_cvt_pk_bf16_f32 v101, v102, v103
	v_cvt_pk_bf16_f32 v102, v104, v105
	v_cvt_pk_bf16_f32 v103, v106, v107
	global_store_dwordx4 v171, v[100:103], s[18:19] nt
	s_add_u32 s14, s14, s26
	s_sub_u32 s3, s3, 1

.Lmoe_dste_6:
	s_add_u32 s18, s6, s23
	s_addc_u32 s19, s7, 0
	ds_write_b128 v172, v[108:111] offset:0
	ds_write_b128 v172, v[112:115] offset:1040
	ds_write_b128 v172, v[116:119] offset:2080
	ds_write_b128 v172, v[120:123] offset:3120
	ds_write_b128 v172, v[124:127] offset:4160
	ds_write_b128 v172, v[128:131] offset:5200
	ds_write_b128 v172, v[132:135] offset:6240
	ds_write_b128 v172, v[136:139] offset:7280
	s_waitcnt lgkmcnt(0)
	ds_read2_b32 v[108:109], v173 offset0:0 offset1:32
	ds_read2_b32 v[110:111], v173 offset0:64 offset1:96
	ds_read2_b32 v[112:113], v173 offset0:128 offset1:160
	ds_read2_b32 v[114:115], v173 offset0:192 offset1:224
	ds_read2_b32 v[116:117], v173 offset0:8 offset1:40
	ds_read2_b32 v[118:119], v173 offset0:72 offset1:104
	ds_read2_b32 v[120:121], v173 offset0:136 offset1:168
	ds_read2_b32 v[122:123], v173 offset0:200 offset1:232
	ds_read2_b32 v[124:125], v173 offset0:16 offset1:48
	ds_read2_b32 v[126:127], v173 offset0:80 offset1:112
	ds_read2_b32 v[128:129], v173 offset0:144 offset1:176
	ds_read2_b32 v[130:131], v173 offset0:208 offset1:240
	s_waitcnt lgkmcnt(8)
	v_cvt_pk_bf16_f32 v108, v108, v109
	v_cvt_pk_bf16_f32 v109, v110, v111
	v_cvt_pk_bf16_f32 v110, v112, v113
	v_cvt_pk_bf16_f32 v111, v114, v115
	global_store_dwordx4 v168, v[108:111], s[18:19] nt
	ds_read2_b32 v[132:133], v173 offset0:24 offset1:56
	ds_read2_b32 v[134:135], v173 offset0:88 offset1:120
	ds_read2_b32 v[136:137], v173 offset0:152 offset1:184
	ds_read2_b32 v[138:139], v173 offset0:216 offset1:248
	s_waitcnt lgkmcnt(8)
	v_cvt_pk_bf16_f32 v116, v116, v117
	v_cvt_pk_bf16_f32 v117, v118, v119
	v_cvt_pk_bf16_f32 v118, v120, v121
	v_cvt_pk_bf16_f32 v119, v122, v123
	global_store_dwordx4 v169, v[116:119], s[18:19] nt
	s_waitcnt lgkmcnt(4)
	v_cvt_pk_bf16_f32 v124, v124, v125
	v_cvt_pk_bf16_f32 v125, v126, v127
	v_cvt_pk_bf16_f32 v126, v128, v129
	v_cvt_pk_bf16_f32 v127, v130, v131
	global_store_dwordx4 v170, v[124:127], s[18:19] nt
	s_waitcnt lgkmcnt(0)
	v_cvt_pk_bf16_f32 v132, v132, v133
	v_cvt_pk_bf16_f32 v133, v134, v135
	v_cvt_pk_bf16_f32 v134, v136, v137
	v_cvt_pk_bf16_f32 v135, v138, v139
	global_store_dwordx4 v171, v[132:135], s[18:19] nt
	s_add_u32 s14, s14, s26
	s_sub_u32 s3, s3, 1

.Lmoe_dste_7:
	s_add_u32 s18, s6, s23
	s_addc_u32 s19, s7, 0
	ds_write_b128 v172, v[224:227] offset:0
	ds_write_b128 v172, v[228:231] offset:1040
	ds_write_b128 v172, v[232:235] offset:2080
	ds_write_b128 v172, v[236:239] offset:3120
	ds_write_b128 v172, v[240:243] offset:4160
	ds_write_b128 v172, v[244:247] offset:5200
	ds_write_b128 v172, v[248:251] offset:6240
	ds_write_b128 v172, v[216:219] offset:7280
	s_waitcnt lgkmcnt(0)
	ds_read2_b32 v[224:225], v173 offset0:0 offset1:32
	ds_read2_b32 v[226:227], v173 offset0:64 offset1:96
	ds_read2_b32 v[228:229], v173 offset0:128 offset1:160
	ds_read2_b32 v[230:231], v173 offset0:192 offset1:224
	ds_read2_b32 v[232:233], v173 offset0:8 offset1:40
	ds_read2_b32 v[234:235], v173 offset0:72 offset1:104
	ds_read2_b32 v[236:237], v173 offset0:136 offset1:168
	ds_read2_b32 v[238:239], v173 offset0:200 offset1:232
	ds_read2_b32 v[240:241], v173 offset0:16 offset1:48
	ds_read2_b32 v[242:243], v173 offset0:80 offset1:112
	ds_read2_b32 v[244:245], v173 offset0:144 offset1:176
	ds_read2_b32 v[246:247], v173 offset0:208 offset1:240
	s_waitcnt lgkmcnt(8)
	v_cvt_pk_bf16_f32 v224, v224, v225
	v_cvt_pk_bf16_f32 v225, v226, v227
	v_cvt_pk_bf16_f32 v226, v228, v229
	v_cvt_pk_bf16_f32 v227, v230, v231
	global_store_dwordx4 v168, v[224:227], s[18:19] nt
	ds_read2_b32 v[248:249], v173 offset0:24 offset1:56
	ds_read2_b32 v[250:251], v173 offset0:88 offset1:120
	ds_read2_b32 v[216:217], v173 offset0:152 offset1:184
	ds_read2_b32 v[218:219], v173 offset0:216 offset1:248
	s_waitcnt lgkmcnt(8)
	v_cvt_pk_bf16_f32 v232, v232, v233
	v_cvt_pk_bf16_f32 v233, v234, v235
	v_cvt_pk_bf16_f32 v234, v236, v237
	v_cvt_pk_bf16_f32 v235, v238, v239
	global_store_dwordx4 v169, v[232:235], s[18:19] nt
	s_waitcnt lgkmcnt(4)
	v_cvt_pk_bf16_f32 v240, v240, v241
	v_cvt_pk_bf16_f32 v241, v242, v243
	v_cvt_pk_bf16_f32 v242, v244, v245
	v_cvt_pk_bf16_f32 v243, v246, v247
	global_store_dwordx4 v170, v[240:243], s[18:19] nt
	s_waitcnt lgkmcnt(0)
	v_cvt_pk_bf16_f32 v248, v248, v249
	v_cvt_pk_bf16_f32 v249, v250, v251
	v_cvt_pk_bf16_f32 v250, v216, v217
	v_cvt_pk_bf16_f32 v251, v218, v219
	global_store_dwordx4 v171, v[248:251], s[18:19] nt
	s_add_u32 s14, s14, s26
	s_sub_u32 s3, s3, 1
	s_branch .Lmoe_drain_loop
.Lmoe_exit:
	s_waitcnt vmcnt(0) lgkmcnt(0)
	s_mov_b64 exec, s[30:31]
	s_cmp_eq_u32 s0, 0
	s_cbranch_scc1 .Lmoe_tail_A
	s_cmp_eq_u32 s0, 1
	s_cbranch_scc1 .Lmoe_tail_B
	s_cmp_eq_u32 s0, 2
	s_cbranch_scc1 .Lmoe_tail_D
	s_cmp_eq_u32 s0, 3
	s_cbranch_scc1 .Lmoe_tail_E
	s_cmp_eq_u32 s0, 4
	s_cbranch_scc1 .Lmoe_tail_T1
	s_cmp_eq_u32 s0, 5
	s_cbranch_scc1 .Lmoe_tail_T2
.Lmoe_tail_T3:
	v_readlane_b32 s0, v255, 0
	v_readlane_b32 s1, v255, 1
	v_readlane_b32 s2, v255, 2
	v_readlane_b32 s3, v255, 3
	v_readlane_b32 s4, v255, 4
	v_readlane_b32 s5, v255, 5
	v_readlane_b32 s6, v255, 6
	v_readlane_b32 s7, v255, 7
	v_readlane_b32 s8, v255, 8
	v_readlane_b32 s9, v255, 9
	v_readlane_b32 s10, v255, 10
	v_readlane_b32 s11, v255, 11
	v_readlane_b32 s12, v255, 12
	v_readlane_b32 s13, v255, 13
	v_readlane_b32 s14, v255, 14
	v_readlane_b32 s15, v255, 15
	v_readlane_b32 s16, v255, 16
	v_readlane_b32 s17, v255, 17
	v_readlane_b32 s18, v255, 18
	v_readlane_b32 s19, v255, 19
	v_readlane_b32 s20, v255, 20
	v_readlane_b32 s21, v255, 21
	v_readlane_b32 s22, v255, 22
	v_readlane_b32 s23, v255, 23
	v_readlane_b32 s24, v255, 24
	v_readlane_b32 s25, v255, 25
	v_readlane_b32 s26, v255, 26
	v_readlane_b32 s27, v255, 27
	v_readlane_b32 s28, v255, 28
	v_readlane_b32 s29, v255, 29
	v_readlane_b32 s30, v255, 30
	v_readlane_b32 s31, v255, 31
	v_readlane_b32 s32, v255, 32
	v_readlane_b32 s33, v255, 33
	v_readlane_b32 s34, v255, 34
	v_readlane_b32 s35, v255, 35
	s_nop 3
	s_branch .Lmoe_exit

.LBB0_2064:
	s_waitcnt vmcnt(0)
	v_readlane_b32 s26, v254, 28
	v_readlane_b32 s27, v254, 29
	s_barrier
.LBB0_2065:
	s_branch .Lmoe_site_T1
.Lmoe_ret_T1:
	s_getreg_b32 s2, hwreg(HW_REG_XCC_ID, 0, 4)
	s_waitcnt vmcnt(0)
	s_waitcnt vmcnt(0)
	s_barrier
	s_mov_b64 s[0:1], exec
	v_readlane_b32 s6, v253, 4
	v_readlane_b32 s7, v253, 5
	s_and_b64 s[6:7], s[0:1], s[6:7]
	s_mov_b64 exec, s[6:7]
	s_cbranch_execz .LBB0_2117
	v_readlane_b32 s3, v252, 34
	s_waitcnt vmcnt(0) expcnt(0) lgkmcnt(0)
	s_and_b32 s2, s2, 15
	v_mov_b32_e32 v2, s3
	ds_read_b32 v5, v2
	v_readlane_b32 s3, v252, 35
	s_waitcnt lgkmcnt(0)
	v_cmp_ne_u32_e32 vcc, 0, v5
	v_mov_b32_e32 v2, s3
	ds_read_b32 v4, v2
	s_cbranch_vccnz .LBB0_2081
	v_readlane_b32 s8, v253, 0
	v_readlane_b32 s9, v253, 1
	s_load_dwordx2 s[6:7], s[8:9], 0x4
	s_mov_b32 s8, 1
	s_waitcnt lgkmcnt(0)
	s_mul_i32 s3, s6, s95
	s_mul_i32 s3, s3, s7
	s_branch .LBB0_2069

.LBB0_2438:
	s_waitcnt vmcnt(0)
	v_readlane_b32 s26, v254, 28
	s_barrier
	v_readlane_b32 s27, v254, 29
.LBB0_2439:
	s_branch .Lmoe_site_T2
.Lmoe_ret_T2:
	s_getreg_b32 s2, hwreg(HW_REG_XCC_ID, 0, 4)
	s_waitcnt vmcnt(0)
	s_waitcnt vmcnt(0)
	s_barrier
	s_mov_b64 s[0:1], exec
	v_readlane_b32 s6, v253, 4
	v_readlane_b32 s7, v253, 5
	s_and_b64 s[6:7], s[0:1], s[6:7]
	s_mov_b64 exec, s[6:7]
	s_cbranch_execz .LBB0_2491
	v_readlane_b32 s3, v252, 34
	s_waitcnt vmcnt(0) expcnt(0) lgkmcnt(0)
	s_and_b32 s2, s2, 15
	v_mov_b32_e32 v2, s3
	ds_read_b32 v5, v2
	v_readlane_b32 s3, v252, 35
	s_waitcnt lgkmcnt(0)
	v_cmp_ne_u32_e32 vcc, 0, v5
	v_mov_b32_e32 v2, s3
	ds_read_b32 v4, v2
	s_cbranch_vccnz .LBB0_2455
	v_readlane_b32 s8, v253, 0
	v_readlane_b32 s9, v253, 1
	s_load_dwordx2 s[6:7], s[8:9], 0x4
	s_mov_b32 s8, 1
	s_waitcnt lgkmcnt(0)
	s_mul_i32 s3, s6, s95
	s_mul_i32 s3, s3, s7
	s_branch .LBB0_2443
